# v43: v34 + router logits: transposing reduction of the 16 partial sums by lane swaps (permlane16/32 swap) and DPP exchanges instead of 17 LDS round trips per expert group; same pairs and tree
# baseline (speedup 1.0000x reference)
; __device__ __forceinline__ void ph9_router(const Frame& F, const Args& A) {
;     ...
;             for (int g = 0; g < 4; ++g) { float q[4][4];
; #pragma unroll
;                 for (int el = 0; el < 4; ++el) { f32x4 a0 = {0.f, 0.f, 0.f, 0.f}, a1 = a0, a2 = a0, a3 = a0;
; #pragma unroll
;                     for (int j = 0; j < 8; ++j) { const f32x4 w = wl[(4 * g + el) * 512 + lane + 64 * j];
;                         a0 += hv[0][j] * w; a1 += hv[1][j] * w; a2 += hv[2][j] * w; a3 += hv[3][j] * w; }
;                     q[0][el] = (a0.x + a0.y) + (a0.z + a0.w); q[1][el] = (a1.x + a1.y) + (a1.z + a1.w); q[2][el] = (a2.x + a2.y) + (a2.z + a2.w); q[3][el] = (a3.x + a3.y) + (a3.z + a3.w); }
.LBB0_1199:
	v_add_u32_e32 v2, s14, v157
	ds_read_b128 v[230:233], v2
	v_cmp_eq_u32_e32 vcc, s14, v158
	s_add_i32 s14, s14, 0x8000
	s_cmp_eq_u32 s14, 0x20000
	ds_read_b128 v[4:7], v2 offset:1024
	s_waitcnt lgkmcnt(1)
	v_pk_fma_f32 v[8:9], v[26:27], v[232:233], 0 op_sel_hi:[1,1,0]
	v_pk_fma_f32 v[144:145], v[30:31], v[230:231], 0 op_sel_hi:[1,1,0]
	v_pk_fma_f32 v[146:147], v[20:21], v[232:233], 0 op_sel_hi:[1,1,0]
	v_pk_fma_f32 v[148:149], v[24:25], v[230:231], 0 op_sel_hi:[1,1,0]
	v_pk_fma_f32 v[150:151], v[14:15], v[232:233], 0 op_sel_hi:[1,1,0]
	v_pk_fma_f32 v[152:153], v[16:17], v[230:231], 0 op_sel_hi:[1,1,0]
	v_pk_fma_f32 v[154:155], v[10:11], v[232:233], 0 op_sel_hi:[1,1,0]
	v_pk_fma_f32 v[160:161], v[12:13], v[230:231], 0 op_sel_hi:[1,1,0]
	ds_read_b128 v[230:233], v2 offset:2048
	s_waitcnt lgkmcnt(1)
	v_pk_fma_f32 v[8:9], v[48:49], v[6:7], v[8:9]
	v_pk_fma_f32 v[144:145], v[52:53], v[4:5], v[144:145]
	v_pk_fma_f32 v[146:147], v[38:39], v[6:7], v[146:147]
	v_pk_fma_f32 v[148:149], v[40:41], v[4:5], v[148:149]
	v_pk_fma_f32 v[150:151], v[28:29], v[6:7], v[150:151]
	v_pk_fma_f32 v[152:153], v[32:33], v[4:5], v[152:153]
	v_pk_fma_f32 v[154:155], v[18:19], v[6:7], v[154:155]
	v_pk_fma_f32 v[160:161], v[22:23], v[4:5], v[160:161]
	ds_read_b128 v[4:7], v2 offset:3072
	s_waitcnt lgkmcnt(1)
	v_pk_fma_f32 v[8:9], v[62:63], v[232:233], v[8:9]
	v_pk_fma_f32 v[144:145], v[64:65], v[230:231], v[144:145]
	v_pk_fma_f32 v[146:147], v[54:55], v[232:233], v[146:147]
	v_pk_fma_f32 v[148:149], v[56:57], v[230:231], v[148:149]
	v_pk_fma_f32 v[150:151], v[42:43], v[232:233], v[150:151]
	v_pk_fma_f32 v[152:153], v[44:45], v[230:231], v[152:153]
	v_pk_fma_f32 v[154:155], v[34:35], v[232:233], v[154:155]
	v_pk_fma_f32 v[160:161], v[36:37], v[230:231], v[160:161]
	ds_read_b128 v[230:233], v2 offset:4096
	s_waitcnt lgkmcnt(1)
	v_pk_fma_f32 v[8:9], v[76:77], v[6:7], v[8:9]
	v_pk_fma_f32 v[144:145], v[80:81], v[4:5], v[144:145]
	v_pk_fma_f32 v[146:147], v[68:69], v[6:7], v[146:147]
	v_pk_fma_f32 v[148:149], v[72:73], v[4:5], v[148:149]
	v_pk_fma_f32 v[150:151], v[58:59], v[6:7], v[150:151]
	v_pk_fma_f32 v[152:153], v[60:61], v[4:5], v[152:153]
	v_pk_fma_f32 v[154:155], v[46:47], v[6:7], v[154:155]
	v_pk_fma_f32 v[160:161], v[50:51], v[4:5], v[160:161]
	ds_read_b128 v[4:7], v2 offset:5120
	s_waitcnt lgkmcnt(1)
	v_pk_fma_f32 v[8:9], v[96:97], v[232:233], v[8:9]
	v_pk_fma_f32 v[144:145], v[100:101], v[230:231], v[144:145]
	v_pk_fma_f32 v[146:147], v[86:87], v[232:233], v[146:147]
	v_pk_fma_f32 v[148:149], v[88:89], v[230:231], v[148:149]
	v_pk_fma_f32 v[150:151], v[74:75], v[232:233], v[150:151]
	v_pk_fma_f32 v[152:153], v[78:79], v[230:231], v[152:153]
	v_pk_fma_f32 v[154:155], v[66:67], v[232:233], v[154:155]
	v_pk_fma_f32 v[160:161], v[70:71], v[230:231], v[160:161]
	ds_read_b128 v[230:233], v2 offset:6144
	s_waitcnt lgkmcnt(1)
	v_pk_fma_f32 v[8:9], v[112:113], v[6:7], v[8:9]
	v_pk_fma_f32 v[144:145], v[116:117], v[4:5], v[144:145]
	v_pk_fma_f32 v[146:147], v[102:103], v[6:7], v[146:147]
	v_pk_fma_f32 v[148:149], v[104:105], v[4:5], v[148:149]
	v_pk_fma_f32 v[150:151], v[90:91], v[6:7], v[150:151]
	v_pk_fma_f32 v[152:153], v[92:93], v[4:5], v[152:153]
	v_pk_fma_f32 v[154:155], v[82:83], v[6:7], v[154:155]
	v_pk_fma_f32 v[160:161], v[84:85], v[4:5], v[160:161]
	ds_read_b128 v[4:7], v2 offset:7168
	s_waitcnt lgkmcnt(1)
	v_pk_fma_f32 v[8:9], v[126:127], v[232:233], v[8:9]
	v_pk_fma_f32 v[144:145], v[128:129], v[230:231], v[144:145]
	v_pk_fma_f32 v[146:147], v[118:119], v[232:233], v[146:147]
	v_pk_fma_f32 v[148:149], v[120:121], v[230:231], v[148:149]
	v_pk_fma_f32 v[150:151], v[106:107], v[232:233], v[150:151]
	v_pk_fma_f32 v[152:153], v[108:109], v[230:231], v[152:153]
	v_pk_fma_f32 v[154:155], v[94:95], v[232:233], v[154:155]
	v_pk_fma_f32 v[160:161], v[98:99], v[230:231], v[160:161]
	s_waitcnt lgkmcnt(0)
	v_pk_fma_f32 v[8:9], v[140:141], v[6:7], v[8:9]
	v_pk_fma_f32 v[144:145], v[142:143], v[4:5], v[144:145]
	v_pk_fma_f32 v[146:147], v[136:137], v[6:7], v[146:147]
	v_pk_fma_f32 v[150:151], v[122:123], v[6:7], v[150:151]
	v_pk_fma_f32 v[6:7], v[110:111], v[6:7], v[154:155]
	v_pk_mov_b32 v[154:155], v[144:145], v[8:9] op_sel:[1,0]
	v_mov_b32_e32 v145, v9
	v_pk_fma_f32 v[148:149], v[138:139], v[4:5], v[148:149]
	v_pk_add_f32 v[8:9], v[154:155], v[144:145]
	v_pk_fma_f32 v[152:153], v[124:125], v[4:5], v[152:153]
	v_pk_fma_f32 v[4:5], v[114:115], v[4:5], v[160:161]
	v_add_f32_e32 v161, v8, v9
	v_pk_mov_b32 v[8:9], v[148:149], v[146:147] op_sel:[1,0]
	v_mov_b32_e32 v149, v147
	v_pk_add_f32 v[8:9], v[8:9], v[148:149]
	s_nop 0
	v_add_f32_e32 v162, v8, v9
	v_pk_mov_b32 v[8:9], v[152:153], v[150:151] op_sel:[1,0]
	v_mov_b32_e32 v153, v151
	v_pk_add_f32 v[8:9], v[8:9], v[152:153]
	s_nop 0
	v_add_f32_e32 v130, v8, v9
	v_pk_mov_b32 v[8:9], v[4:5], v[6:7] op_sel:[1,0]
	v_mov_b32_e32 v5, v7
	v_pk_add_f32 v[4:5], v[8:9], v[4:5]
	s_nop 0
	v_add_f32_e32 v160, v4, v5
	ds_read_b128 v[230:233], v2 offset:8192
	ds_read_b128 v[4:7], v2 offset:9216
	s_waitcnt lgkmcnt(1)
	v_pk_fma_f32 v[8:9], v[26:27], v[232:233], 0 op_sel_hi:[1,1,0]
	v_pk_fma_f32 v[144:145], v[30:31], v[230:231], 0 op_sel_hi:[1,1,0]
	v_pk_fma_f32 v[146:147], v[20:21], v[232:233], 0 op_sel_hi:[1,1,0]
	v_pk_fma_f32 v[148:149], v[24:25], v[230:231], 0 op_sel_hi:[1,1,0]
	v_pk_fma_f32 v[150:151], v[14:15], v[232:233], 0 op_sel_hi:[1,1,0]
	v_pk_fma_f32 v[152:153], v[16:17], v[230:231], 0 op_sel_hi:[1,1,0]
	v_pk_fma_f32 v[154:155], v[10:11], v[232:233], 0 op_sel_hi:[1,1,0]
	v_pk_fma_f32 v[164:165], v[12:13], v[230:231], 0 op_sel_hi:[1,1,0]
	ds_read_b128 v[230:233], v2 offset:10240
	s_waitcnt lgkmcnt(1)
; __device__ __forceinline__ void ph9_router(const Frame& F, const Args& A) {
;     ...
;                 for (int el = 0; el < 4; ++el) { f32x4 a0 = {0.f, 0.f, 0.f, 0.f}, a1 = a0, a2 = a0, a3 = a0;
; #pragma unroll
;                     for (int j = 0; j < 8; ++j) { const f32x4 w = wl[(4 * g + el) * 512 + lane + 64 * j];
;                         a0 += hv[0][j] * w; a1 += hv[1][j] * w; a2 += hv[2][j] * w; a3 += hv[3][j] * w; }
;                     q[0][el] = (a0.x + a0.y) + (a0.z + a0.w); q[1][el] = (a1.x + a1.y) + (a1.z + a1.w); q[2][el] = (a2.x + a2.y) + (a2.z + a2.w); q[3][el] = (a3.x + a3.y) + (a3.z + a3.w); }
	v_pk_fma_f32 v[8:9], v[48:49], v[6:7], v[8:9]
	v_pk_fma_f32 v[144:145], v[52:53], v[4:5], v[144:145]
	v_pk_fma_f32 v[146:147], v[38:39], v[6:7], v[146:147]
	v_pk_fma_f32 v[148:149], v[40:41], v[4:5], v[148:149]
	v_pk_fma_f32 v[150:151], v[28:29], v[6:7], v[150:151]
	v_pk_fma_f32 v[152:153], v[32:33], v[4:5], v[152:153]
	v_pk_fma_f32 v[154:155], v[18:19], v[6:7], v[154:155]
	v_pk_fma_f32 v[164:165], v[22:23], v[4:5], v[164:165]
	ds_read_b128 v[4:7], v2 offset:11264
	s_waitcnt lgkmcnt(1)
	v_pk_fma_f32 v[8:9], v[62:63], v[232:233], v[8:9]
	v_pk_fma_f32 v[144:145], v[64:65], v[230:231], v[144:145]
	v_pk_fma_f32 v[146:147], v[54:55], v[232:233], v[146:147]
	v_pk_fma_f32 v[148:149], v[56:57], v[230:231], v[148:149]
	v_pk_fma_f32 v[150:151], v[42:43], v[232:233], v[150:151]
	v_pk_fma_f32 v[152:153], v[44:45], v[230:231], v[152:153]
	v_pk_fma_f32 v[154:155], v[34:35], v[232:233], v[154:155]
	v_pk_fma_f32 v[164:165], v[36:37], v[230:231], v[164:165]
	ds_read_b128 v[230:233], v2 offset:12288
	s_waitcnt lgkmcnt(1)
	v_pk_fma_f32 v[8:9], v[76:77], v[6:7], v[8:9]
	v_pk_fma_f32 v[144:145], v[80:81], v[4:5], v[144:145]
	v_pk_fma_f32 v[146:147], v[68:69], v[6:7], v[146:147]
	v_pk_fma_f32 v[148:149], v[72:73], v[4:5], v[148:149]
	v_pk_fma_f32 v[150:151], v[58:59], v[6:7], v[150:151]
	v_pk_fma_f32 v[152:153], v[60:61], v[4:5], v[152:153]
	v_pk_fma_f32 v[154:155], v[46:47], v[6:7], v[154:155]
	v_pk_fma_f32 v[164:165], v[50:51], v[4:5], v[164:165]
	ds_read_b128 v[4:7], v2 offset:13312
	s_waitcnt lgkmcnt(1)
	v_pk_fma_f32 v[8:9], v[96:97], v[232:233], v[8:9]
	v_pk_fma_f32 v[144:145], v[100:101], v[230:231], v[144:145]
	v_pk_fma_f32 v[146:147], v[86:87], v[232:233], v[146:147]
	v_pk_fma_f32 v[148:149], v[88:89], v[230:231], v[148:149]
	v_pk_fma_f32 v[150:151], v[74:75], v[232:233], v[150:151]
	v_pk_fma_f32 v[152:153], v[78:79], v[230:231], v[152:153]
	v_pk_fma_f32 v[154:155], v[66:67], v[232:233], v[154:155]
	v_pk_fma_f32 v[164:165], v[70:71], v[230:231], v[164:165]
	ds_read_b128 v[230:233], v2 offset:14336
	s_waitcnt lgkmcnt(1)
	v_pk_fma_f32 v[8:9], v[112:113], v[6:7], v[8:9]
	v_pk_fma_f32 v[144:145], v[116:117], v[4:5], v[144:145]
	v_pk_fma_f32 v[146:147], v[102:103], v[6:7], v[146:147]
	v_pk_fma_f32 v[148:149], v[104:105], v[4:5], v[148:149]
	v_pk_fma_f32 v[150:151], v[90:91], v[6:7], v[150:151]
	v_pk_fma_f32 v[152:153], v[92:93], v[4:5], v[152:153]
	v_pk_fma_f32 v[154:155], v[82:83], v[6:7], v[154:155]
	v_pk_fma_f32 v[164:165], v[84:85], v[4:5], v[164:165]
	ds_read_b128 v[4:7], v2 offset:15360
	s_waitcnt lgkmcnt(1)
	v_pk_fma_f32 v[8:9], v[126:127], v[232:233], v[8:9]
	v_pk_fma_f32 v[144:145], v[128:129], v[230:231], v[144:145]
	v_pk_fma_f32 v[146:147], v[118:119], v[232:233], v[146:147]
	v_pk_fma_f32 v[148:149], v[120:121], v[230:231], v[148:149]
	v_pk_fma_f32 v[150:151], v[106:107], v[232:233], v[150:151]
	v_pk_fma_f32 v[152:153], v[108:109], v[230:231], v[152:153]
	v_pk_fma_f32 v[154:155], v[94:95], v[232:233], v[154:155]
	v_pk_fma_f32 v[164:165], v[98:99], v[230:231], v[164:165]
	s_waitcnt lgkmcnt(0)
	v_pk_fma_f32 v[8:9], v[140:141], v[6:7], v[8:9]
	v_pk_fma_f32 v[144:145], v[142:143], v[4:5], v[144:145]
	v_pk_fma_f32 v[146:147], v[136:137], v[6:7], v[146:147]
	v_pk_fma_f32 v[150:151], v[122:123], v[6:7], v[150:151]
	v_pk_fma_f32 v[6:7], v[110:111], v[6:7], v[154:155]
	v_pk_mov_b32 v[154:155], v[144:145], v[8:9] op_sel:[1,0]
	v_mov_b32_e32 v145, v9
	v_pk_fma_f32 v[148:149], v[138:139], v[4:5], v[148:149]
	v_pk_add_f32 v[8:9], v[154:155], v[144:145]
	v_pk_fma_f32 v[152:153], v[124:125], v[4:5], v[152:153]
	v_pk_fma_f32 v[4:5], v[114:115], v[4:5], v[164:165]
	v_add_f32_e32 v165, v8, v9
	v_pk_mov_b32 v[8:9], v[148:149], v[146:147] op_sel:[1,0]
	v_mov_b32_e32 v149, v147
	v_pk_add_f32 v[8:9], v[8:9], v[148:149]
	s_nop 0
	v_add_f32_e32 v166, v8, v9
	v_pk_mov_b32 v[8:9], v[152:153], v[150:151] op_sel:[1,0]
	v_mov_b32_e32 v153, v151
	v_pk_add_f32 v[8:9], v[8:9], v[152:153]
	s_nop 0
	v_add_f32_e32 v163, v8, v9
	v_pk_mov_b32 v[8:9], v[4:5], v[6:7] op_sel:[1,0]
	v_mov_b32_e32 v5, v7
	v_pk_add_f32 v[4:5], v[8:9], v[4:5]
	s_nop 0
	v_add_f32_e32 v164, v4, v5
	ds_read_b128 v[230:233], v2 offset:16384
	ds_read_b128 v[4:7], v2 offset:17408
	s_waitcnt lgkmcnt(1)
	v_pk_fma_f32 v[8:9], v[26:27], v[232:233], 0 op_sel_hi:[1,1,0]
	v_pk_fma_f32 v[144:145], v[30:31], v[230:231], 0 op_sel_hi:[1,1,0]
	v_pk_fma_f32 v[146:147], v[20:21], v[232:233], 0 op_sel_hi:[1,1,0]
	v_pk_fma_f32 v[148:149], v[24:25], v[230:231], 0 op_sel_hi:[1,1,0]
	v_pk_fma_f32 v[150:151], v[14:15], v[232:233], 0 op_sel_hi:[1,1,0]
	v_pk_fma_f32 v[152:153], v[16:17], v[230:231], 0 op_sel_hi:[1,1,0]
	v_pk_fma_f32 v[154:155], v[10:11], v[232:233], 0 op_sel_hi:[1,1,0]
	v_pk_fma_f32 v[174:175], v[12:13], v[230:231], 0 op_sel_hi:[1,1,0]
	ds_read_b128 v[230:233], v2 offset:18432
	s_waitcnt lgkmcnt(1)
	v_pk_fma_f32 v[8:9], v[48:49], v[6:7], v[8:9]
	v_pk_fma_f32 v[144:145], v[52:53], v[4:5], v[144:145]
	v_pk_fma_f32 v[146:147], v[38:39], v[6:7], v[146:147]
	v_pk_fma_f32 v[148:149], v[40:41], v[4:5], v[148:149]
	v_pk_fma_f32 v[150:151], v[28:29], v[6:7], v[150:151]
	v_pk_fma_f32 v[152:153], v[32:33], v[4:5], v[152:153]
	v_pk_fma_f32 v[154:155], v[18:19], v[6:7], v[154:155]
	v_pk_fma_f32 v[174:175], v[22:23], v[4:5], v[174:175]
	ds_read_b128 v[4:7], v2 offset:19456
	s_waitcnt lgkmcnt(1)
	v_pk_fma_f32 v[8:9], v[62:63], v[232:233], v[8:9]
	v_pk_fma_f32 v[144:145], v[64:65], v[230:231], v[144:145]
	v_pk_fma_f32 v[146:147], v[54:55], v[232:233], v[146:147]
	v_pk_fma_f32 v[148:149], v[56:57], v[230:231], v[148:149]
	v_pk_fma_f32 v[150:151], v[42:43], v[232:233], v[150:151]
	v_pk_fma_f32 v[152:153], v[44:45], v[230:231], v[152:153]
	v_pk_fma_f32 v[154:155], v[34:35], v[232:233], v[154:155]
	v_pk_fma_f32 v[174:175], v[36:37], v[230:231], v[174:175]
	ds_read_b128 v[230:233], v2 offset:20480
	s_waitcnt lgkmcnt(1)
; __device__ __forceinline__ void ph9_router(const Frame& F, const Args& A) {
;     ...
;                 for (int el = 0; el < 4; ++el) { f32x4 a0 = {0.f, 0.f, 0.f, 0.f}, a1 = a0, a2 = a0, a3 = a0;
; #pragma unroll
;                     for (int j = 0; j < 8; ++j) { const f32x4 w = wl[(4 * g + el) * 512 + lane + 64 * j];
;                         a0 += hv[0][j] * w; a1 += hv[1][j] * w; a2 += hv[2][j] * w; a3 += hv[3][j] * w; }
;                     q[0][el] = (a0.x + a0.y) + (a0.z + a0.w); q[1][el] = (a1.x + a1.y) + (a1.z + a1.w); q[2][el] = (a2.x + a2.y) + (a2.z + a2.w); q[3][el] = (a3.x + a3.y) + (a3.z + a3.w); }
	v_pk_fma_f32 v[8:9], v[76:77], v[6:7], v[8:9]
	v_pk_fma_f32 v[144:145], v[80:81], v[4:5], v[144:145]
	v_pk_fma_f32 v[146:147], v[68:69], v[6:7], v[146:147]
	v_pk_fma_f32 v[148:149], v[72:73], v[4:5], v[148:149]
	v_pk_fma_f32 v[150:151], v[58:59], v[6:7], v[150:151]
	v_pk_fma_f32 v[152:153], v[60:61], v[4:5], v[152:153]
	v_pk_fma_f32 v[154:155], v[46:47], v[6:7], v[154:155]
	v_pk_fma_f32 v[174:175], v[50:51], v[4:5], v[174:175]
	ds_read_b128 v[4:7], v2 offset:21504
	s_waitcnt lgkmcnt(1)
	v_pk_fma_f32 v[8:9], v[96:97], v[232:233], v[8:9]
	v_pk_fma_f32 v[144:145], v[100:101], v[230:231], v[144:145]
	v_pk_fma_f32 v[146:147], v[86:87], v[232:233], v[146:147]
	v_pk_fma_f32 v[148:149], v[88:89], v[230:231], v[148:149]
	v_pk_fma_f32 v[150:151], v[74:75], v[232:233], v[150:151]
	v_pk_fma_f32 v[152:153], v[78:79], v[230:231], v[152:153]
	v_pk_fma_f32 v[154:155], v[66:67], v[232:233], v[154:155]
	v_pk_fma_f32 v[174:175], v[70:71], v[230:231], v[174:175]
	ds_read_b128 v[230:233], v2 offset:22528
	s_waitcnt lgkmcnt(1)
	v_pk_fma_f32 v[8:9], v[112:113], v[6:7], v[8:9]
	v_pk_fma_f32 v[144:145], v[116:117], v[4:5], v[144:145]
	v_pk_fma_f32 v[146:147], v[102:103], v[6:7], v[146:147]
	v_pk_fma_f32 v[148:149], v[104:105], v[4:5], v[148:149]
	v_pk_fma_f32 v[150:151], v[90:91], v[6:7], v[150:151]
	v_pk_fma_f32 v[152:153], v[92:93], v[4:5], v[152:153]
	v_pk_fma_f32 v[154:155], v[82:83], v[6:7], v[154:155]
	v_pk_fma_f32 v[174:175], v[84:85], v[4:5], v[174:175]
	ds_read_b128 v[4:7], v2 offset:23552
	s_waitcnt lgkmcnt(1)
	v_pk_fma_f32 v[8:9], v[126:127], v[232:233], v[8:9]
	v_pk_fma_f32 v[144:145], v[128:129], v[230:231], v[144:145]
	v_pk_fma_f32 v[146:147], v[118:119], v[232:233], v[146:147]
	v_pk_fma_f32 v[148:149], v[120:121], v[230:231], v[148:149]
	v_pk_fma_f32 v[150:151], v[106:107], v[232:233], v[150:151]
	v_pk_fma_f32 v[152:153], v[108:109], v[230:231], v[152:153]
	v_pk_fma_f32 v[154:155], v[94:95], v[232:233], v[154:155]
	v_pk_fma_f32 v[174:175], v[98:99], v[230:231], v[174:175]
	s_waitcnt lgkmcnt(0)
	v_pk_fma_f32 v[8:9], v[140:141], v[6:7], v[8:9]
	v_pk_fma_f32 v[144:145], v[142:143], v[4:5], v[144:145]
	v_pk_fma_f32 v[146:147], v[136:137], v[6:7], v[146:147]
	v_pk_fma_f32 v[150:151], v[122:123], v[6:7], v[150:151]
	v_pk_fma_f32 v[6:7], v[110:111], v[6:7], v[154:155]
	v_pk_mov_b32 v[154:155], v[144:145], v[8:9] op_sel:[1,0]
	v_mov_b32_e32 v145, v9
	v_pk_fma_f32 v[148:149], v[138:139], v[4:5], v[148:149]
	v_pk_add_f32 v[8:9], v[154:155], v[144:145]
	v_pk_fma_f32 v[152:153], v[124:125], v[4:5], v[152:153]
	v_add_f32_e32 v170, v8, v9
	v_pk_mov_b32 v[8:9], v[148:149], v[146:147] op_sel:[1,0]
	v_mov_b32_e32 v149, v147
	v_pk_add_f32 v[8:9], v[8:9], v[148:149]
	v_pk_fma_f32 v[4:5], v[114:115], v[4:5], v[174:175]
	v_add_f32_e32 v172, v8, v9
	v_pk_mov_b32 v[8:9], v[152:153], v[150:151] op_sel:[1,0]
	v_mov_b32_e32 v153, v151
	v_pk_add_f32 v[8:9], v[8:9], v[152:153]
	s_nop 0
	v_add_f32_e32 v167, v8, v9
	v_pk_mov_b32 v[8:9], v[4:5], v[6:7] op_sel:[1,0]
	v_mov_b32_e32 v5, v7
	v_pk_add_f32 v[4:5], v[8:9], v[4:5]
	s_nop 0
	v_add_f32_e32 v168, v4, v5
	ds_read_b128 v[230:233], v2 offset:24576
	ds_read_b128 v[4:7], v2 offset:25600
	s_waitcnt lgkmcnt(1)
	v_pk_fma_f32 v[8:9], v[26:27], v[232:233], 0 op_sel_hi:[1,1,0]
	v_pk_fma_f32 v[144:145], v[30:31], v[230:231], 0 op_sel_hi:[1,1,0]
	v_pk_fma_f32 v[146:147], v[20:21], v[232:233], 0 op_sel_hi:[1,1,0]
	v_pk_fma_f32 v[148:149], v[24:25], v[230:231], 0 op_sel_hi:[1,1,0]
	v_pk_fma_f32 v[150:151], v[14:15], v[232:233], 0 op_sel_hi:[1,1,0]
	v_pk_fma_f32 v[152:153], v[16:17], v[230:231], 0 op_sel_hi:[1,1,0]
	v_pk_fma_f32 v[154:155], v[10:11], v[232:233], 0 op_sel_hi:[1,1,0]
	v_pk_fma_f32 v[174:175], v[12:13], v[230:231], 0 op_sel_hi:[1,1,0]
	ds_read_b128 v[230:233], v2 offset:26624
	s_waitcnt lgkmcnt(1)
	v_pk_fma_f32 v[8:9], v[48:49], v[6:7], v[8:9]
	v_pk_fma_f32 v[144:145], v[52:53], v[4:5], v[144:145]
	v_pk_fma_f32 v[146:147], v[38:39], v[6:7], v[146:147]
	v_pk_fma_f32 v[148:149], v[40:41], v[4:5], v[148:149]
	v_pk_fma_f32 v[150:151], v[28:29], v[6:7], v[150:151]
	v_pk_fma_f32 v[152:153], v[32:33], v[4:5], v[152:153]
	v_pk_fma_f32 v[154:155], v[18:19], v[6:7], v[154:155]
	v_pk_fma_f32 v[174:175], v[22:23], v[4:5], v[174:175]
	ds_read_b128 v[4:7], v2 offset:27648
	s_waitcnt lgkmcnt(1)
	v_pk_fma_f32 v[8:9], v[62:63], v[232:233], v[8:9]
	v_pk_fma_f32 v[144:145], v[64:65], v[230:231], v[144:145]
	v_pk_fma_f32 v[146:147], v[54:55], v[232:233], v[146:147]
	v_pk_fma_f32 v[148:149], v[56:57], v[230:231], v[148:149]
	v_pk_fma_f32 v[150:151], v[42:43], v[232:233], v[150:151]
	v_pk_fma_f32 v[152:153], v[44:45], v[230:231], v[152:153]
	v_pk_fma_f32 v[154:155], v[34:35], v[232:233], v[154:155]
	v_pk_fma_f32 v[174:175], v[36:37], v[230:231], v[174:175]
	ds_read_b128 v[230:233], v2 offset:28672
	s_waitcnt lgkmcnt(1)
; __device__ __forceinline__ void ph9_router(const Frame& F, const Args& A) {
;     ...
;                 for (int el = 0; el < 4; ++el) { f32x4 a0 = {0.f, 0.f, 0.f, 0.f}, a1 = a0, a2 = a0, a3 = a0;
; #pragma unroll
;                     for (int j = 0; j < 8; ++j) { const f32x4 w = wl[(4 * g + el) * 512 + lane + 64 * j];
;                         a0 += hv[0][j] * w; a1 += hv[1][j] * w; a2 += hv[2][j] * w; a3 += hv[3][j] * w; }
;                     q[0][el] = (a0.x + a0.y) + (a0.z + a0.w); q[1][el] = (a1.x + a1.y) + (a1.z + a1.w); q[2][el] = (a2.x + a2.y) + (a2.z + a2.w); q[3][el] = (a3.x + a3.y) + (a3.z + a3.w); }
;                 float s1[2][4], s2[4], s3[2];
; #pragma unroll
;                 for (int k = 0; k < 2; ++k)
; #pragma unroll
;                     for (int el = 0; el < 4; ++el) { const float keep = b4 ? q[2 * k + 1][el] : q[2 * k][el], send = b4 ? q[2 * k][el] : q[2 * k + 1][el]; s1[k][el] = keep + __shfl_xor(send, 16); }
; #pragma unroll
;                 for (int el = 0; el < 4; ++el) { const float keep = b5 ? s1[1][el] : s1[0][el], send = b5 ? s1[0][el] : s1[1][el]; s2[el] = keep + __shfl_xor(send, 32); }
; #pragma unroll
;                 for (int k = 0; k < 2; ++k) { const float keep = b0 ? s2[2 * k + 1] : s2[2 * k], send = b0 ? s2[2 * k] : s2[2 * k + 1]; s3[k] = keep + __shfl_xor(send, 1); }
;                 float s4; { const float keep = b1 ? s3[1] : s3[0], send = b1 ? s3[0] : s3[1]; s4 = keep + __shfl_xor(send, 2); }
;                 s4 += __shfl_xor(s4, 4); s4 += __shfl_xor(s4, 8);
;                 if (((lane >> 2) & 3) == g) mine = s4; }
	v_pk_fma_f32 v[8:9], v[76:77], v[6:7], v[8:9]
	v_pk_fma_f32 v[144:145], v[80:81], v[4:5], v[144:145]
	v_pk_fma_f32 v[146:147], v[68:69], v[6:7], v[146:147]
	v_pk_fma_f32 v[148:149], v[72:73], v[4:5], v[148:149]
	v_pk_fma_f32 v[150:151], v[58:59], v[6:7], v[150:151]
	v_pk_fma_f32 v[152:153], v[60:61], v[4:5], v[152:153]
	v_pk_fma_f32 v[154:155], v[46:47], v[6:7], v[154:155]
	v_pk_fma_f32 v[174:175], v[50:51], v[4:5], v[174:175]
	s_waitcnt lgkmcnt(0)
	v_pk_fma_f32 v[8:9], v[96:97], v[232:233], v[8:9]
	v_pk_fma_f32 v[144:145], v[100:101], v[230:231], v[144:145]
	v_pk_fma_f32 v[146:147], v[86:87], v[232:233], v[146:147]
	v_pk_fma_f32 v[148:149], v[88:89], v[230:231], v[148:149]
	v_pk_fma_f32 v[150:151], v[74:75], v[232:233], v[150:151]
	v_pk_fma_f32 v[152:153], v[78:79], v[230:231], v[152:153]
	v_pk_fma_f32 v[154:155], v[66:67], v[232:233], v[154:155]
	v_pk_fma_f32 v[174:175], v[70:71], v[230:231], v[174:175]
	ds_read_b128 v[4:7], v2 offset:29696
	s_waitcnt lgkmcnt(0)
	v_pk_fma_f32 v[144:145], v[116:117], v[4:5], v[144:145]
	v_pk_fma_f32 v[148:149], v[104:105], v[4:5], v[148:149]
	v_pk_fma_f32 v[152:153], v[92:93], v[4:5], v[152:153]
	v_pk_fma_f32 v[4:5], v[84:85], v[4:5], v[174:175]
	ds_read_b128 v[174:177], v2 offset:30720
	v_pk_fma_f32 v[8:9], v[112:113], v[6:7], v[8:9]
	v_pk_fma_f32 v[146:147], v[102:103], v[6:7], v[146:147]
	v_pk_fma_f32 v[150:151], v[90:91], v[6:7], v[150:151]
	v_pk_fma_f32 v[154:155], v[82:83], v[6:7], v[154:155]
	s_waitcnt lgkmcnt(0)
	v_pk_fma_f32 v[6:7], v[126:127], v[176:177], v[8:9]
	v_pk_fma_f32 v[8:9], v[128:129], v[174:175], v[144:145]
	v_pk_fma_f32 v[144:145], v[118:119], v[176:177], v[146:147]
	v_pk_fma_f32 v[146:147], v[120:121], v[174:175], v[148:149]
	v_pk_fma_f32 v[148:149], v[106:107], v[176:177], v[150:151]
	v_pk_fma_f32 v[150:151], v[108:109], v[174:175], v[152:153]
	v_pk_fma_f32 v[152:153], v[94:95], v[176:177], v[154:155]
	v_pk_fma_f32 v[154:155], v[98:99], v[174:175], v[4:5]
	ds_read_b128 v[2:5], v2 offset:31744
	s_waitcnt lgkmcnt(0)
	v_pk_fma_f32 v[6:7], v[140:141], v[4:5], v[6:7]
	v_pk_fma_f32 v[8:9], v[142:143], v[2:3], v[8:9]
	v_pk_fma_f32 v[144:145], v[136:137], v[4:5], v[144:145]
	v_pk_fma_f32 v[148:149], v[122:123], v[4:5], v[148:149]
	v_pk_fma_f32 v[4:5], v[110:111], v[4:5], v[152:153]
	v_pk_mov_b32 v[152:153], v[8:9], v[6:7] op_sel:[1,0]
	v_mov_b32_e32 v9, v7
	v_pk_fma_f32 v[146:147], v[138:139], v[2:3], v[146:147]
	v_pk_add_f32 v[6:7], v[152:153], v[8:9]
	v_pk_fma_f32 v[150:151], v[124:125], v[2:3], v[150:151]
	v_add_f32_e32 v8, v6, v7
	v_pk_mov_b32 v[6:7], v[146:147], v[144:145] op_sel:[1,0]
	v_mov_b32_e32 v147, v145
	v_pk_add_f32 v[6:7], v[6:7], v[146:147]
	v_pk_fma_f32 v[2:3], v[114:115], v[2:3], v[154:155]
	v_add_f32_e32 v9, v6, v7
	v_pk_mov_b32 v[6:7], v[150:151], v[148:149] op_sel:[1,0]
	v_mov_b32_e32 v151, v149
	v_pk_add_f32 v[6:7], v[6:7], v[150:151]
	s_nop 0
	v_add_f32_e32 v144, v6, v7
	v_pk_mov_b32 v[6:7], v[2:3], v[4:5] op_sel:[1,0]
	v_mov_b32_e32 v3, v5
	v_pk_add_f32 v[2:3], v[6:7], v[2:3]
	v_add_f32_e32 v2, v2, v3
	s_nop 1
	v_permlane16_swap_b32_e32 v161, v162
	v_permlane16_swap_b32_e32 v165, v166
	v_permlane16_swap_b32_e32 v170, v172
	v_permlane16_swap_b32_e32 v8, v9
	v_permlane16_swap_b32_e32 v130, v160
	v_permlane16_swap_b32_e32 v163, v164
	v_permlane16_swap_b32_e32 v167, v168
	v_permlane16_swap_b32_e32 v144, v2
	s_nop 1
	v_add_f32_e32 v3, v161, v162
	v_add_f32_e32 v4, v165, v166
	v_add_f32_e32 v5, v170, v172
	v_add_f32_e32 v6, v8, v9
	v_add_f32_e32 v7, v130, v160
	v_add_f32_e32 v8, v163, v164
	v_add_f32_e32 v9, v167, v168
	v_add_f32_e32 v2, v144, v2
	s_nop 1
	v_permlane32_swap_b32_e32 v3, v7
	v_permlane32_swap_b32_e32 v4, v8
	v_permlane32_swap_b32_e32 v5, v9
	v_permlane32_swap_b32_e32 v6, v2
	s_nop 1
	v_add_f32_e32 v3, v3, v7
	v_add_f32_e32 v4, v4, v8
	v_add_f32_e32 v5, v5, v9
	v_add_f32_e32 v2, v6, v2
	v_cndmask_b32_e64 v6, v4, v3, s[4:5]
	v_cndmask_b32_e64 v7, v3, v4, s[4:5]
	v_cndmask_b32_e64 v8, v2, v5, s[4:5]
	v_cndmask_b32_e64 v9, v5, v2, s[4:5]
	s_nop 1
	v_add_f32_dpp v3, v7, v6 quad_perm:[1,0,3,2] row_mask:0xf bank_mask:0xf
	v_add_f32_dpp v2, v9, v8 quad_perm:[1,0,3,2] row_mask:0xf bank_mask:0xf
	v_cndmask_b32_e64 v4, v2, v3, s[6:7]
	v_cndmask_b32_e64 v5, v3, v2, s[6:7]
	s_nop 1
	v_add_f32_dpp v2, v5, v4 quad_perm:[2,3,0,1] row_mask:0xf bank_mask:0xf
	s_nop 1
	v_mov_b32_dpp v3, v2 row_half_mirror row_mask:0xf bank_mask:0xf
	s_nop 1
	v_add_f32_dpp v2, v3, v2 quad_perm:[3,2,1,0] row_mask:0xf bank_mask:0xf
	s_nop 1
	v_add_f32_dpp v2, v2, v2 row_ror:8 row_mask:0xf bank_mask:0xf
	s_nop 1
	v_cndmask_b32_e32 v159, v159, v2, vcc
	s_cbranch_scc0 .LBB0_1199
	v_or_b32_e32 v130, s42, v156
	v_lshl_add_u64 v[2:3], v[130:131], 2, s[74:75]
	global_load_dword v2, v[2:3], off
	s_mov_b32 s42, 16
	s_and_b64 vcc, exec, s[12:13]
	s_waitcnt vmcnt(0)
	v_add_f32_e32 v2, v159, v2
	v_cndmask_b32_e64 v191, v191, v2, s[0:1]
	v_cndmask_b32_e64 v190, v2, v190, s[0:1]
	s_mov_b64 s[0:1], 0
	s_cbranch_vccnz .LBB0_1202
	s_mov_b64 s[12:13], -1
	s_branch .LBB0_1196
